# MoE GEMMs: expert of each row tile found with one lane-parallel compare and s_bcnt1 instead of a 32-step compare / add-carry chain
# speedup vs baseline: 1.0461x; 1.0042x over previous
;     __device__ __forceinline__ bool next(int i, Unit& u) const { u.aux = 0; return t.map(i, u.pm, u.pn); }
;     __device__ __forceinline__ bool next(int i, Unit& u) const { u.aux = i & 1; return t.map(i >> 1, u.pm, u.pn); }
;     __device__ __forceinline__ bool map(int i, int& pm, int& pn) const {
;         const long L = (long)i * G + c; if (L >= nwg) return false;
;         int wgid = (int)L; { const int q = nwg / NXCD, r = nwg % NXCD, xcd = wgid % NXCD, off = wgid / NXCD; wgid = (xcd < r ? xcd * (q + 1) : r * (q + 1) + (xcd - r) * q) + off; }
;         const int nig = WGM * nN, gid = wgid / nig, fm = gid * WGM, gsz = (nM - fm) < WGM ? (nM - fm) : WGM;
;         pm = fm + ((wgid % nig) % gsz); pn = (wgid % nig) / gsz; return true;
;     __device__ __forceinline__ bool next(int i, Unit& u) const {
;         if (!t.map(i, u.pm, u.pn)) return false;
;         const int row0 = u.pm * BM; int e = 0;
; #pragma unroll
;         for (int j = 0; j < 32; ++j) e += (pad_end[j] <= row0) ? 1 : 0;
;         u.aux = __builtin_amdgcn_readfirstlane(e < 31 ? e : 31); return true;
.LBB0_1646:
	s_add_i32 s36, s36, 1
	s_mul_i32 s2, s36, s69
	s_mul_hi_u32 s3, s36, s84
	s_add_i32 s3, s3, s2
	s_mul_i32 s2, s36, s84
	v_readlane_b32 s4, v255, 0
	s_add_u32 s2, s2, s4
	s_addc_u32 s3, s3, s17
	v_cmp_ge_i64_e32 vcc, s[2:3], v[146:147]
	v_cmp_lt_i64_e64 s[4:5], s[2:3], v[146:147]
	s_cbranch_vccnz .LBB0_1648
	s_ashr_i32 s3, s2, 31
	s_lshr_b32 s3, s3, 29
	s_add_i32 s3, s2, s3
	s_ashr_i32 s51, s3, 3
	s_and_b32 s3, s3, -8
	s_sub_i32 s2, s2, s3
	s_cmp_lt_i32 s2, 0
	s_cselect_b32 s3, s18, s16
	s_mul_i32 s2, s3, s2
	s_add_i32 s2, s2, s51
	s_ashr_i32 s3, s2, 31
	s_lshr_b32 s3, s3, 25
	s_add_i32 s3, s2, s3
	s_ashr_i32 s51, s3, 7
	s_lshl_b32 s52, s51, 3
	s_sub_i32 s51, s13, s52
	s_min_i32 s53, s51, 8
	s_abs_i32 s51, s53
	v_cvt_f32_u32_e32 v2, s51
	s_sub_i32 s58, 0, s51
	s_and_b32 s3, s3, 0xffffff80
	s_sub_i32 s2, s2, s3
	v_rcp_iflag_f32_e32 v2, v2
	s_abs_i32 s3, s2
	s_xor_b32 s57, s2, s53
	s_ashr_i32 s57, s57, 31
	v_mul_f32_e32 v2, 0x4f7ffffe, v2
	v_cvt_u32_f32_e32 v2, v2
	v_mov_b32_e32 v6, s20
	ds_read_b128 v[6:9], v6
	v_readfirstlane_b32 s59, v2
	s_mul_i32 s58, s58, s59
	s_mul_hi_u32 s58, s59, s58
	s_add_i32 s59, s59, s58
	s_mul_hi_u32 s58, s3, s59
	s_mul_i32 s59, s58, s51
	s_sub_i32 s3, s3, s59
	s_add_i32 s60, s58, 1
	s_sub_i32 s59, s3, s51
	s_cmp_ge_u32 s3, s51
	s_cselect_b32 s58, s60, s58
	s_cselect_b32 s3, s59, s3
	s_add_i32 s59, s58, 1
	s_cmp_ge_u32 s3, s51
	s_cselect_b32 s3, s59, s58
	s_xor_b32 s3, s3, s57
	v_mov_b32_e32 v2, s19
	s_sub_i32 s67, s3, s57
	ds_read_b128 v[2:5], v2
	s_mul_i32 s3, s67, s53
	s_sub_i32 s2, s2, s3
	s_add_i32 s86, s2, s52
	s_lshl_b32 s2, s86, 8
	s_waitcnt lgkmcnt(0)
	v_mbcnt_lo_u32_b32 v2, -1, 0
	v_lshl_add_u32 v2, v2, 2, s19
	ds_read_b32 v2, v2
	s_waitcnt lgkmcnt(0)
	v_cmp_ge_i32_e32 vcc, s2, v2
	s_nop 1
	s_bcnt1_i32_b32 s87, vcc_lo
	s_min_i32 s87, s87, 31

;     __device__ __forceinline__ bool next(int i, Unit& u) const { u.aux = 0; return t.map(i, u.pm, u.pn); }
;     __device__ __forceinline__ bool next(int i, Unit& u) const { u.aux = i & 1; return t.map(i >> 1, u.pm, u.pn); }
;     __device__ __forceinline__ bool map(int i, int& pm, int& pn) const {
;         const long L = (long)i * G + c; if (L >= nwg) return false;
;         int wgid = (int)L; { const int q = nwg / NXCD, r = nwg % NXCD, xcd = wgid % NXCD, off = wgid / NXCD; wgid = (xcd < r ? xcd * (q + 1) : r * (q + 1) + (xcd - r) * q) + off; }
;         const int nig = WGM * nN, gid = wgid / nig, fm = gid * WGM, gsz = (nM - fm) < WGM ? (nM - fm) : WGM;
;         pm = fm + ((wgid % nig) % gsz); pn = (wgid % nig) / gsz; return true;
;     __device__ __forceinline__ bool next(int i, Unit& u) const {
;         if (!t.map(i, u.pm, u.pn)) return false;
;         const int row0 = u.pm * BM; int e = 0;
; #pragma unroll
;         for (int j = 0; j < 32; ++j) e += (pad_end[j] <= row0) ? 1 : 0;
;         u.aux = __builtin_amdgcn_readfirstlane(e < 31 ? e : 31); return true;
.LBB0_1720:
	s_add_i32 s23, s23, 1
	s_mul_i32 s2, s23, s33
	s_mul_hi_u32 s3, s23, s84
	s_add_i32 s3, s3, s2
	s_mul_i32 s2, s23, s84
	v_readlane_b32 s4, v255, 0
	s_add_u32 s2, s2, s4
	s_addc_u32 s3, s3, s34
	v_cmp_ge_i64_e32 vcc, s[2:3], v[252:253]
	v_cmp_lt_i64_e64 s[4:5], s[2:3], v[252:253]
	s_cbranch_vccnz .LBB0_1722
	s_ashr_i32 s3, s2, 31
	s_lshr_b32 s3, s3, 29
	s_add_i32 s3, s2, s3
	s_ashr_i32 s43, s3, 3
	s_and_b32 s3, s3, -8
	s_sub_i32 s2, s2, s3
	s_lshr_b32 s3, s2, 31
	s_add_i32 s3, s3, s14
	s_mul_i32 s2, s3, s2
	s_add_i32 s2, s2, s43
	s_ashr_i32 s3, s2, 31
	s_lshr_b32 s3, s3, 26
	s_add_i32 s3, s2, s3
	s_ashr_i32 s43, s3, 6
	s_lshl_b32 s44, s43, 3
	s_sub_i32 s43, s14, s44
	s_min_i32 s45, s43, 8
	s_abs_i32 s43, s45
	v_cvt_f32_u32_e32 v2, s43
	s_sub_i32 s47, 0, s43
	s_andn2_b32 s3, s3, 63
	s_sub_i32 s2, s2, s3
	v_rcp_iflag_f32_e32 v2, v2
	s_abs_i32 s3, s2
	s_xor_b32 s46, s2, s45
	s_ashr_i32 s46, s46, 31
	v_mul_f32_e32 v2, 0x4f7ffffe, v2
	v_cvt_u32_f32_e32 v2, v2
	v_mov_b32_e32 v6, s36
	ds_read_b128 v[6:9], v6
	v_readfirstlane_b32 s51, v2
	s_mul_i32 s47, s47, s51
	s_mul_hi_u32 s47, s51, s47
	s_add_i32 s51, s51, s47
	s_mul_hi_u32 s47, s3, s51
	s_mul_i32 s51, s47, s43
	s_sub_i32 s3, s3, s51
	s_add_i32 s52, s47, 1
	s_sub_i32 s51, s3, s43
	s_cmp_ge_u32 s3, s43
	s_cselect_b32 s47, s52, s47
	s_cselect_b32 s3, s51, s3
	s_add_i32 s51, s47, 1
	s_cmp_ge_u32 s3, s43
	s_cselect_b32 s3, s51, s47
	s_xor_b32 s3, s3, s46
	v_mov_b32_e32 v2, s35
	s_sub_i32 s43, s3, s46
	ds_read_b128 v[2:5], v2
	s_mul_i32 s3, s43, s45
	s_sub_i32 s2, s2, s3
	s_add_i32 s44, s2, s44
	s_lshl_b32 s2, s44, 8
	s_waitcnt lgkmcnt(0)
	v_mbcnt_lo_u32_b32 v2, -1, 0
	v_lshl_add_u32 v2, v2, 2, s35
	ds_read_b32 v2, v2
	s_waitcnt lgkmcnt(0)
	v_cmp_ge_i32_e32 vcc, s2, v2
	s_nop 1
	s_bcnt1_i32_b32 s45, vcc_lo
	s_min_i32 s45, s45, 31
